# P13 sparse attention: static s_setprio 1 for waves 4-7 during the phase
# baseline (speedup 1.0000x reference)
.LBB0_2742:
	v_readfirstlane_b32 s0, v0
	s_lshr_b32 s0, s0, 8
	s_cmp_lg_u32 s0, 0
	s_cbranch_scc0 .Lprio13_skip
	s_setprio 1

.LBB0_2903:
	s_setprio 0
	s_cmp_lt_i32 s68, 15
	s_cselect_b64 s[0:1], -1, 0
	s_cmp_gt_i32 s69, 14
	s_cselect_b64 s[2:3], -1, 0
	s_and_b64 s[0:1], s[0:1], s[2:3]
	s_andn2_b64 vcc, exec, s[0:1]
	s_cbranch_vccnz .LBB0_2982
	s_cmpk_gt_i32 s58, 0x3ff
	v_readfirstlane_b32 s3, v0
	s_cbranch_scc1 .LBB0_2928
	s_ashr_i32 s24, s58, 31
	s_lshr_b32 s0, s24, 29
	s_add_i32 s5, s58, s0
	s_and_b32 s0, s5, -8
	s_sub_i32 s4, s58, s0
	s_cmp_gt_i32 s4, -1
	s_cbranch_scc0 .LBB0_2907
	s_lshl_b32 s2, s4, 7
	s_ashr_i32 s0, s5, 3
	s_cbranch_execz .LBB0_2908
	s_branch .LBB0_2909
